# v16 + attention unit-end store drain before the LDS-release barrier removed + diff copies 2-4 late DMA point after 2nd QK MFMA
# speedup vs baseline: 1.0037x; 1.0037x over previous
; #define DMA_WAIT(last) do { if (last) asm volatile("s_waitcnt vmcnt(0)" ::: "memory"); else asm volatile("s_waitcnt vmcnt(%0)" :: "n"(NPW) : "memory"); } while (0)
; template <int DK>
; __device__ __forceinline__ void qkt(f32x16& p0, f32x16& p1, const char* Ks, const bf16x8* qr, int r32, int hi) {
;   p0 = f32x16{}; p1 = f32x16{};
; #pragma unroll
;   for (int d0 = 0; d0 < DK / 16; ++d0) { const int cb = (d0 * 16 + hi * 8) * 2;
;     const bf16x8 b0 = *reinterpret_cast<const bf16x8*>(Ks + ATT_KSWZ(r32, cb));
;     const bf16x8 b1 = *reinterpret_cast<const bf16x8*>(Ks + ATT_KSWZ(32 + r32, cb));
;     p0 = __builtin_amdgcn_mfma_f32_32x32x16_bf16(b0, qr[d0], p0, 0, 0, 0);
;     p1 = __builtin_amdgcn_mfma_f32_32x32x16_bf16(b1, qr[d0], p1, 0, 0, 0);
;   }
; }
; template <int DK, int DV, bool OFF, class QLoader> ...
;     ...
;   f32x16 pA0, pA1, pB0, pB1; bf16x8 pa0, pa1, pa2, pa3; const int NT = nkeys / KVBLK;
;   DMA_TILE(0, 0); DMA_TILE(1, 1); DMA_WAIT(false); __syncthreads(); if (2 < NT) DMA_TILE(2, 2);
;   qkt<DK>(pA0, pA1, K_lds, qr, r32, hi); partialSM<DK, OFF>(pA0, pA1, negMC);
.LBB0_863:
	ds_read_b128 v[66:69], v162 offset:32768
	ds_read_b128 v[70:73], v162 offset:36864
	ds_read_b128 v[130:133], v164 offset:32768
	ds_read_b128 v[134:137], v164 offset:36864
	v_exp_f32_e32 v82, v82
	v_add_f32_e32 v180, 0, v197
	v_add_f32_e32 v180, v200, v180
	v_add_f32_e32 v180, v198, v180
	v_add_f32_e32 v180, v202, v180
	v_add_f32_e32 v180, v204, v180
	v_add_f32_e32 v180, v207, v180
	v_add_f32_e32 v180, v205, v180
	v_add_f32_e32 v180, v210, v180
	v_add_f32_e32 v180, v199, v180
	v_add_f32_e32 v180, v203, v180
	v_add_f32_e32 v180, v201, v180
	v_add_f32_e32 v180, v209, v180
	v_add_f32_e32 v180, v206, v180
	v_add_f32_e32 v180, v211, v180
	v_add_f32_e32 v180, v208, v180
	v_add_f32_e32 v180, v212, v180
	s_waitcnt lgkmcnt(0)
	v_mfma_f32_32x32x16_bf16 v[98:113], v[66:69], v[114:117], 0
	v_exp_f32_e32 v83, v83
	v_exp_f32_e32 v84, v84
	v_exp_f32_e32 v85, v85
	v_exp_f32_e32 v86, v86
	v_exp_f32_e32 v87, v87
	v_exp_f32_e32 v88, v88
	v_exp_f32_e32 v89, v89
	v_mfma_f32_32x32x16_bf16 v[66:81], v[70:73], v[114:117], 0
	s_cmp_eq_u32 s80, 0
	s_cbranch_scc1 .Lstg_l2
	s_add_i32 s32, s55, -2
	s_cmp_ge_u32 s32, s95
	s_cbranch_scc1 .Lstg_l2
	s_add_u32 s98, s76, 0x1ec08000
	s_addc_u32 s99, s77, 0
	s_mov_b32 m0, s81
	s_nop 0
	global_load_lds_dwordx4 v0, s[98:99]
	s_add_u32 s98, s78, 0xdc01000
	s_addc_u32 s99, s79, 0
	s_mov_b32 m0, s82
	s_nop 0
	global_load_lds_dwordx4 v232, s[98:99]
	s_add_u32 s98, s98, 0x80
	s_addc_u32 s99, s99, 0
	s_mov_b32 m0, s84
	s_nop 0
	global_load_lds_dwordx4 v232, s[98:99]
; __device__ __forceinline__ void finishSM(f32x16& p0, f32x16& p1, float& l_reg, bf16x8& pa0, bf16x8& pa1, bf16x8& pa2, bf16x8& pa3) {
; #pragma unroll
;   for (int r = 0; r < 16; ++r) p1[r] = __builtin_amdgcn_exp2f(p1[r]);
;   float ps = 0;
; #pragma unroll
;   for (int r = 0; r < 16; ++r) ps += p0[r];
; #pragma unroll
;   for (int r = 0; r < 16; ++r) ps += p1[r];
;   l_reg += ps;
;     ...
;   ATT_PK4(p0, 0, pa0); ATT_PK4(p0, 8, pa1); ATT_PK4(p1, 0, pa2); ATT_PK4(p1, 8, pa3);
;     ...
; }
; template <int DK>
; __device__ __forceinline__ void qkt(f32x16& p0, f32x16& p1, const char* Ks, const bf16x8* qr, int r32, int hi) {
;   p0 = f32x16{}; p1 = f32x16{};
; #pragma unroll
;   for (int d0 = 0; d0 < DK / 16; ++d0) { const int cb = (d0 * 16 + hi * 8) * 2;
;     const bf16x8 b0 = *reinterpret_cast<const bf16x8*>(Ks + ATT_KSWZ(r32, cb));
;     const bf16x8 b1 = *reinterpret_cast<const bf16x8*>(Ks + ATT_KSWZ(32 + r32, cb));
;     p0 = __builtin_amdgcn_mfma_f32_32x32x16_bf16(b0, qr[d0], p0, 0, 0, 0);
;     p1 = __builtin_amdgcn_mfma_f32_32x32x16_bf16(b1, qr[d0], p1, 0, 0, 0);
;   }
; }
; template <int DV, int GRP> __device__ __forceinline__ void v_group_read(s16x4* vf, int vb) {
;   sfor<0, 8>([&](auto ic) { constexpr int j = decltype(ic)::value; vf[j] = tr_read<v_rd_off<DV>(GRP, j / 2, j % 2)>(vb); });
; }
; __device__ __forceinline__ void pv_group(f32x16& od, const s16x4* vf, bf16x8 pa0, bf16x8 pa1, bf16x8 pa2, bf16x8 pa3) {
;     ...
;   od = __builtin_amdgcn_mfma_f32_32x32x16_bf16(pa0, ATT_PK(vf[0], vf[1]), od, 0, 0, 0);
;   od = __builtin_amdgcn_mfma_f32_32x32x16_bf16(pa1, ATT_PK(vf[2], vf[3]), od, 0, 0, 0);
;   od = __builtin_amdgcn_mfma_f32_32x32x16_bf16(pa2, ATT_PK(vf[4], vf[5]), od, 0, 0, 0);
;   od = __builtin_amdgcn_mfma_f32_32x32x16_bf16(pa3, ATT_PK(vf[6], vf[7]), od, 0, 0, 0);
;     ...
; }
; template <int DV> __device__ __forceinline__ void pv_all_pipe(f32x16* o, int vb, bf16x8 pa0, bf16x8 pa1, bf16x8 pa2, bf16x8 pa3) {
;   s16x4 va[8], vc[8];
;   v_group_read<DV, 0>(va, vb); v_group_read<DV, 1>(vc, vb);
;   lgkm_wait8<8>(va); pv_group(o[0], va, pa0, pa1, pa2, pa3);
;   if constexpr (DV == 128) {
;     s16x4 vd[8], ve[8];
;     v_group_read<DV, 2>(vd, vb);
;     lgkm_wait8<8>(vc); pv_group(o[1], vc, pa0, pa1, pa2, pa3);
;     v_group_read<DV, 3>(ve, vb);
;     lgkm_wait8<8>(vd); pv_group(o[2], vd, pa0, pa1, pa2, pa3);
;     lgkm_wait8<0>(ve); pv_group(o[3], ve, pa0, pa1, pa2, pa3);
.Lstg_l2:
	v_exp_f32_e32 v90, v90
	v_exp_f32_e32 v91, v91
	v_exp_f32_e32 v92, v92
	v_exp_f32_e32 v93, v93
	v_exp_f32_e32 v94, v94
	v_exp_f32_e32 v95, v95
	v_exp_f32_e32 v96, v96
	v_mfma_f32_32x32x16_bf16 v[98:113], v[130:133], v[118:121], v[98:113]
	v_exp_f32_e32 v97, v97
	v_mfma_f32_32x32x16_bf16 v[66:81], v[134:137], v[118:121], v[66:81]
	ds_read_b128 v[130:133], v166 offset:32768
	ds_read_b128 v[134:137], v166 offset:36864
	v_add_f32_e32 v180, v82, v180
	v_add_f32_e32 v180, v83, v180
	v_add_f32_e32 v180, v84, v180
	v_add_f32_e32 v180, v85, v180
	v_add_f32_e32 v180, v86, v180
	v_add_f32_e32 v180, v87, v180
	v_add_f32_e32 v180, v88, v180
	v_add_f32_e32 v180, v89, v180
	s_waitcnt lgkmcnt(0)
	v_mfma_f32_32x32x16_bf16 v[98:113], v[130:133], v[122:125], v[98:113]
	v_mfma_f32_32x32x16_bf16 v[66:81], v[134:137], v[122:125], v[66:81]
	ds_read_b128 v[130:133], v168 offset:32768
	ds_read_b128 v[134:137], v168 offset:36864
	v_add_f32_e32 v180, v90, v180
	v_add_f32_e32 v180, v91, v180
	v_add_f32_e32 v180, v92, v180
	v_add_f32_e32 v180, v93, v180
	v_add_f32_e32 v180, v94, v180
	v_add_f32_e32 v180, v95, v180
	v_add_f32_e32 v180, v96, v180
	v_add_f32_e32 v180, v97, v180
	s_waitcnt lgkmcnt(0)
	v_mfma_f32_32x32x16_bf16 v[98:113], v[130:133], v[126:129], v[98:113]
	v_mfma_f32_32x32x16_bf16 v[66:81], v[134:137], v[126:129], v[66:81]
	v_add_f32_e32 v172, v172, v180
	v_cvt_pk_bf16_f32 v130, v197, v200
	v_cvt_pk_bf16_f32 v131, v198, v202
	v_cvt_pk_bf16_f32 v132, v204, v207
	v_cvt_pk_bf16_f32 v133, v205, v210
	v_cvt_pk_bf16_f32 v134, v199, v203
	v_cvt_pk_bf16_f32 v135, v201, v209
	v_cvt_pk_bf16_f32 v136, v206, v211
	v_cvt_pk_bf16_f32 v137, v208, v212
	v_cvt_pk_bf16_f32 v138, v82, v83
	v_cvt_pk_bf16_f32 v139, v84, v85
	v_cvt_pk_bf16_f32 v140, v86, v87
	v_cvt_pk_bf16_f32 v141, v88, v89
	v_cvt_pk_bf16_f32 v142, v90, v91
	v_cvt_pk_bf16_f32 v143, v92, v93
	v_cvt_pk_bf16_f32 v144, v94, v95
	v_cvt_pk_bf16_f32 v145, v96, v97
	ds_read_b64_tr_b16 v[174:175], v170 offset:0
	ds_read_b64_tr_b16 v[176:177], v170 offset:0x800
	ds_read_b64_tr_b16 v[184:185], v170 offset:0x1000
	ds_read_b64_tr_b16 v[186:187], v170 offset:0x1800
	ds_read_b64_tr_b16 v[188:189], v170 offset:0x2000
	ds_read_b64_tr_b16 v[190:191], v170 offset:0x2800
	ds_read_b64_tr_b16 v[192:193], v170 offset:0x3000
	ds_read_b64_tr_b16 v[194:195], v170 offset:0x3800
	ds_read_b64_tr_b16 v[214:215], v170 offset:0x200
	ds_read_b64_tr_b16 v[216:217], v170 offset:0xa00
	ds_read_b64_tr_b16 v[218:219], v170 offset:0x1200
	s_nop 0
	v_permlane32_swap_b32_e32 v130, v132
	v_permlane32_swap_b32_e32 v131, v133
	ds_read_b64_tr_b16 v[220:221], v170 offset:0x1a00
	ds_read_b64_tr_b16 v[222:223], v170 offset:0x2200
	ds_read_b64_tr_b16 v[224:225], v170 offset:0x2a00
	ds_read_b64_tr_b16 v[226:227], v170 offset:0x3200
	ds_read_b64_tr_b16 v[228:229], v170 offset:0x3a00
	s_waitcnt lgkmcnt(8)
	v_permlane32_swap_b32_e32 v134, v136
	s_nop 0
	v_mfma_f32_32x32x16_bf16 v[2:17], v[130:133], v[174:177], v[2:17]
	v_permlane32_swap_b32_e32 v135, v137
	v_permlane32_swap_b32_e32 v138, v140
	v_permlane32_swap_b32_e32 v139, v141
	ds_read_b64_tr_b16 v[174:175], v170 offset:0x400
	v_mfma_f32_32x32x16_bf16 v[2:17], v[134:137], v[184:187], v[2:17]
	v_permlane32_swap_b32_e32 v142, v144
	v_permlane32_swap_b32_e32 v143, v145
	ds_read_b64_tr_b16 v[176:177], v170 offset:0xc00
	ds_read_b64_tr_b16 v[184:185], v170 offset:0x1400
	ds_read_b64_tr_b16 v[186:187], v170 offset:0x1c00
	v_mfma_f32_32x32x16_bf16 v[2:17], v[138:141], v[188:191], v[2:17]
	ds_read_b64_tr_b16 v[188:189], v170 offset:0x2400
	ds_read_b64_tr_b16 v[190:191], v170 offset:0x2c00
	v_exp_f32_e32 v173, v98
	v_exp_f32_e32 v196, v113
	v_mfma_f32_32x32x16_bf16 v[2:17], v[142:145], v[192:195], v[2:17]
	ds_read_b64_tr_b16 v[192:193], v170 offset:0x3400
	ds_read_b64_tr_b16 v[194:195], v170 offset:0x3c00
	s_waitcnt lgkmcnt(8)
	s_nop 0
	v_mfma_f32_32x32x16_bf16 v[50:65], v[130:133], v[214:217], v[50:65]
	ds_read_b64_tr_b16 v[214:215], v170 offset:0x600
	ds_read_b64_tr_b16 v[216:217], v170 offset:0xe00
	v_mfma_f32_32x32x16_bf16 v[50:65], v[134:137], v[218:221], v[50:65]
	ds_read_b64_tr_b16 v[218:219], v170 offset:0x1600
	ds_read_b64_tr_b16 v[220:221], v170 offset:0x1e00
	v_mfma_f32_32x32x16_bf16 v[50:65], v[138:141], v[222:225], v[50:65]
	ds_read_b64_tr_b16 v[222:223], v170 offset:0x2600
	ds_read_b64_tr_b16 v[224:225], v170 offset:0x2e00
	v_mfma_f32_32x32x16_bf16 v[50:65], v[142:145], v[226:229], v[50:65]
	ds_read_b64_tr_b16 v[226:227], v170 offset:0x3600
	ds_read_b64_tr_b16 v[228:229], v170 offset:0x3e00
	s_waitcnt lgkmcnt(8)
	s_nop 0
	s_waitcnt lgkmcnt(0)
	v_mfma_f32_32x32x16_bf16 v[34:49], v[130:133], v[174:177], v[34:49]
	v_exp_f32_e32 v174, v99
	v_exp_f32_e32 v175, v100
	v_mfma_f32_32x32x16_bf16 v[18:33], v[130:133], v[214:217], v[18:33]
	v_mfma_f32_32x32x16_bf16 v[34:49], v[134:137], v[184:187], v[34:49]
	v_exp_f32_e32 v184, v101
	v_exp_f32_e32 v185, v102
	v_exp_f32_e32 v186, v103
	v_exp_f32_e32 v187, v104
	v_mfma_f32_32x32x16_bf16 v[18:33], v[134:137], v[218:221], v[18:33]
	v_mfma_f32_32x32x16_bf16 v[34:49], v[138:141], v[188:191], v[34:49]
	v_exp_f32_e32 v188, v105
	v_exp_f32_e32 v189, v106
	v_exp_f32_e32 v190, v107
	v_exp_f32_e32 v191, v108
	v_mfma_f32_32x32x16_bf16 v[18:33], v[138:141], v[222:225], v[18:33]
	v_mfma_f32_32x32x16_bf16 v[34:49], v[142:145], v[192:195], v[34:49]
	v_exp_f32_e32 v192, v109
	v_exp_f32_e32 v193, v110
	v_exp_f32_e32 v194, v111
	v_exp_f32_e32 v195, v112
	v_mfma_f32_32x32x16_bf16 v[18:33], v[142:145], v[226:229], v[18:33]
	s_andn2_b64 vcc, exec, s[24:25]
	s_cbranch_vccz .LBB0_866

; __device__ __forceinline__ void finishSM(f32x16& p0, f32x16& p1, float& l_reg, bf16x8& pa0, bf16x8& pa1, bf16x8& pa2, bf16x8& pa3) {
; #pragma unroll
;   for (int r = 0; r < 16; ++r) p1[r] = __builtin_amdgcn_exp2f(p1[r]);
;   float ps = 0;
; #pragma unroll
;   for (int r = 0; r < 16; ++r) ps += p0[r];
; #pragma unroll
;   for (int r = 0; r < 16; ++r) ps += p1[r];
;   l_reg += ps;
;     ...
;   ATT_PK4(p0, 0, pa0); ATT_PK4(p0, 8, pa1); ATT_PK4(p1, 0, pa2); ATT_PK4(p1, 8, pa3);
;     ...
; }
; template <int DK>
; __device__ __forceinline__ void qkt(f32x16& p0, f32x16& p1, const char* Ks, const bf16x8* qr, int r32, int hi) {
;   p0 = f32x16{}; p1 = f32x16{};
; #pragma unroll
;   for (int d0 = 0; d0 < DK / 16; ++d0) { const int cb = (d0 * 16 + hi * 8) * 2;
;     const bf16x8 b0 = *reinterpret_cast<const bf16x8*>(Ks + ATT_KSWZ(r32, cb));
;     const bf16x8 b1 = *reinterpret_cast<const bf16x8*>(Ks + ATT_KSWZ(32 + r32, cb));
;     p0 = __builtin_amdgcn_mfma_f32_32x32x16_bf16(b0, qr[d0], p0, 0, 0, 0);
;     p1 = __builtin_amdgcn_mfma_f32_32x32x16_bf16(b1, qr[d0], p1, 0, 0, 0);
;   }
; }
; template <int DV, int GRP> __device__ __forceinline__ void v_group_read(s16x4* vf, int vb) {
;   sfor<0, 8>([&](auto ic) { constexpr int j = decltype(ic)::value; vf[j] = tr_read<v_rd_off<DV>(GRP, j / 2, j % 2)>(vb); });
; }
; __device__ __forceinline__ void pv_group(f32x16& od, const s16x4* vf, bf16x8 pa0, bf16x8 pa1, bf16x8 pa2, bf16x8 pa3) {
;     ...
;   od = __builtin_amdgcn_mfma_f32_32x32x16_bf16(pa0, ATT_PK(vf[0], vf[1]), od, 0, 0, 0);
;   od = __builtin_amdgcn_mfma_f32_32x32x16_bf16(pa1, ATT_PK(vf[2], vf[3]), od, 0, 0, 0);
;   od = __builtin_amdgcn_mfma_f32_32x32x16_bf16(pa2, ATT_PK(vf[4], vf[5]), od, 0, 0, 0);
;   od = __builtin_amdgcn_mfma_f32_32x32x16_bf16(pa3, ATT_PK(vf[6], vf[7]), od, 0, 0, 0);
;     ...
; }
; template <int DV> __device__ __forceinline__ void pv_all_pipe(f32x16* o, int vb, bf16x8 pa0, bf16x8 pa1, bf16x8 pa2, bf16x8 pa3) {
;   s16x4 va[8], vc[8];
;   v_group_read<DV, 0>(va, vb); v_group_read<DV, 1>(vc, vb);
;   lgkm_wait8<8>(va); pv_group(o[0], va, pa0, pa1, pa2, pa3);
;   if constexpr (DV == 128) {
;     s16x4 vd[8], ve[8];
;     v_group_read<DV, 2>(vd, vb);
;     lgkm_wait8<8>(vc); pv_group(o[1], vc, pa0, pa1, pa2, pa3);
;     v_group_read<DV, 3>(ve, vb);
;     lgkm_wait8<8>(vd); pv_group(o[2], vd, pa0, pa1, pa2, pa3);
;     lgkm_wait8<0>(ve); pv_group(o[3], ve, pa0, pa1, pa2, pa3);
.LBB0_872:
	ds_read_b128 v[82:85], v162 offset:49152
	ds_read_b128 v[86:89], v162 offset:53248
	ds_read_b128 v[130:133], v164 offset:49152
	ds_read_b128 v[134:137], v164 offset:53248
	v_exp_f32_e32 v66, v66
	v_add_f32_e32 v180, 0, v173
	v_add_f32_e32 v180, v174, v180
	v_add_f32_e32 v180, v175, v180
	v_add_f32_e32 v180, v184, v180
	v_add_f32_e32 v180, v185, v180
	v_add_f32_e32 v180, v186, v180
	v_add_f32_e32 v180, v187, v180
	v_add_f32_e32 v180, v188, v180
	v_add_f32_e32 v180, v189, v180
	v_add_f32_e32 v180, v190, v180
	v_add_f32_e32 v180, v191, v180
	v_add_f32_e32 v180, v192, v180
	v_add_f32_e32 v180, v193, v180
	v_add_f32_e32 v180, v194, v180
	v_add_f32_e32 v180, v195, v180
	v_add_f32_e32 v180, v196, v180
	s_waitcnt lgkmcnt(0)
	v_mfma_f32_32x32x16_bf16 v[98:113], v[82:85], v[114:117], 0
	v_exp_f32_e32 v67, v67
	v_exp_f32_e32 v68, v68
	v_exp_f32_e32 v69, v69
	v_exp_f32_e32 v70, v70
	v_exp_f32_e32 v71, v71
	v_exp_f32_e32 v72, v72
	v_exp_f32_e32 v73, v73
	v_mfma_f32_32x32x16_bf16 v[82:97], v[86:89], v[114:117], 0
	s_cmp_eq_u32 s80, 0
	s_cbranch_scc1 .Lstg_l3
	s_add_i32 s32, s55, -1
	s_cmp_ge_u32 s32, s95
	s_cbranch_scc1 .Lstg_l3
	s_add_u32 s98, s76, 0x1ec0a000
	s_addc_u32 s99, s77, 0
	s_mov_b32 m0, s85
	s_nop 0
	global_load_lds_dwordx4 v0, s[98:99]
	s_add_u32 s98, s78, 0xdc61000
	s_addc_u32 s99, s79, 0
	s_mov_b32 m0, s87
	s_nop 0
	global_load_lds_dwordx4 v232, s[98:99]
	s_add_u32 s98, s98, 0x80
	s_addc_u32 s99, s99, 0
	s_mov_b32 m0, s88
	s_nop 0
	global_load_lds_dwordx4 v232, s[98:99]
.Lstg_l3:
	v_exp_f32_e32 v74, v74
	v_exp_f32_e32 v75, v75
	v_exp_f32_e32 v76, v76
	v_exp_f32_e32 v77, v77
	v_exp_f32_e32 v78, v78
	v_exp_f32_e32 v79, v79
	v_exp_f32_e32 v80, v80
	v_mfma_f32_32x32x16_bf16 v[98:113], v[130:133], v[118:121], v[98:113]
	v_exp_f32_e32 v81, v81
	v_mfma_f32_32x32x16_bf16 v[82:97], v[134:137], v[118:121], v[82:97]
	ds_read_b128 v[130:133], v166 offset:49152
	ds_read_b128 v[134:137], v166 offset:53248
	v_add_f32_e32 v180, v66, v180
	v_add_f32_e32 v180, v67, v180
	v_add_f32_e32 v180, v68, v180
	v_add_f32_e32 v180, v69, v180
	v_add_f32_e32 v180, v70, v180
	v_add_f32_e32 v180, v71, v180
	v_add_f32_e32 v180, v72, v180
	v_add_f32_e32 v180, v73, v180
	s_waitcnt lgkmcnt(0)
	v_mfma_f32_32x32x16_bf16 v[98:113], v[130:133], v[122:125], v[98:113]
	v_mfma_f32_32x32x16_bf16 v[82:97], v[134:137], v[122:125], v[82:97]
	ds_read_b128 v[130:133], v168 offset:49152
	ds_read_b128 v[134:137], v168 offset:53248
	v_add_f32_e32 v180, v74, v180
	v_add_f32_e32 v180, v75, v180
	v_add_f32_e32 v180, v76, v180
	v_add_f32_e32 v180, v77, v180
	v_add_f32_e32 v180, v78, v180
	v_add_f32_e32 v180, v79, v180
	v_add_f32_e32 v180, v80, v180
	v_add_f32_e32 v180, v81, v180
	s_waitcnt lgkmcnt(0)
	v_mfma_f32_32x32x16_bf16 v[98:113], v[130:133], v[126:129], v[98:113]
	v_mfma_f32_32x32x16_bf16 v[82:97], v[134:137], v[126:129], v[82:97]
	v_add_f32_e32 v172, v172, v180
	v_cvt_pk_bf16_f32 v130, v173, v174
	v_cvt_pk_bf16_f32 v131, v175, v184
	v_cvt_pk_bf16_f32 v132, v185, v186
	v_cvt_pk_bf16_f32 v133, v187, v188
	v_cvt_pk_bf16_f32 v134, v189, v190
	v_cvt_pk_bf16_f32 v135, v191, v192
	v_cvt_pk_bf16_f32 v136, v193, v194
	v_cvt_pk_bf16_f32 v137, v195, v196
	v_cvt_pk_bf16_f32 v138, v66, v67
	v_cvt_pk_bf16_f32 v139, v68, v69
	v_cvt_pk_bf16_f32 v140, v70, v71
	v_cvt_pk_bf16_f32 v141, v72, v73
	v_cvt_pk_bf16_f32 v142, v74, v75
	v_cvt_pk_bf16_f32 v143, v76, v77
	v_cvt_pk_bf16_f32 v144, v78, v79
	v_cvt_pk_bf16_f32 v145, v80, v81
	ds_read_b64_tr_b16 v[176:177], v171 offset:0
	ds_read_b64_tr_b16 v[178:179], v171 offset:0x800
	ds_read_b64_tr_b16 v[198:199], v171 offset:0x1000
	ds_read_b64_tr_b16 v[200:201], v171 offset:0x1800
	ds_read_b64_tr_b16 v[202:203], v171 offset:0x2000
	ds_read_b64_tr_b16 v[204:205], v171 offset:0x2800
	ds_read_b64_tr_b16 v[206:207], v171 offset:0x3000
	ds_read_b64_tr_b16 v[208:209], v171 offset:0x3800
	ds_read_b64_tr_b16 v[210:211], v171 offset:0x200
	ds_read_b64_tr_b16 v[212:213], v171 offset:0xa00
	ds_read_b64_tr_b16 v[214:215], v171 offset:0x1200
	s_nop 0
	v_permlane32_swap_b32_e32 v130, v132
	v_permlane32_swap_b32_e32 v131, v133
	ds_read_b64_tr_b16 v[216:217], v171 offset:0x1a00
	ds_read_b64_tr_b16 v[218:219], v171 offset:0x2200
	ds_read_b64_tr_b16 v[220:221], v171 offset:0x2a00
	ds_read_b64_tr_b16 v[222:223], v171 offset:0x3200
	ds_read_b64_tr_b16 v[224:225], v171 offset:0x3a00
	s_waitcnt lgkmcnt(8)
	v_permlane32_swap_b32_e32 v134, v136
	s_nop 0
	v_mfma_f32_32x32x16_bf16 v[2:17], v[130:133], v[176:179], v[2:17]
	v_permlane32_swap_b32_e32 v135, v137
	v_permlane32_swap_b32_e32 v138, v140
	v_permlane32_swap_b32_e32 v139, v141
	ds_read_b64_tr_b16 v[176:177], v171 offset:0x400
	v_mfma_f32_32x32x16_bf16 v[2:17], v[134:137], v[198:201], v[2:17]
	v_permlane32_swap_b32_e32 v142, v144
	v_permlane32_swap_b32_e32 v143, v145
	ds_read_b64_tr_b16 v[178:179], v171 offset:0xc00
	ds_read_b64_tr_b16 v[198:199], v171 offset:0x1400
	ds_read_b64_tr_b16 v[200:201], v171 offset:0x1c00
	v_mfma_f32_32x32x16_bf16 v[2:17], v[138:141], v[202:205], v[2:17]
	ds_read_b64_tr_b16 v[202:203], v171 offset:0x2400
	ds_read_b64_tr_b16 v[204:205], v171 offset:0x2c00
	v_exp_f32_e32 v197, v98
	v_mfma_f32_32x32x16_bf16 v[2:17], v[142:145], v[206:209], v[2:17]
	ds_read_b64_tr_b16 v[206:207], v171 offset:0x3400
	ds_read_b64_tr_b16 v[208:209], v171 offset:0x3c00
	s_waitcnt lgkmcnt(8)
	s_nop 0
	v_mfma_f32_32x32x16_bf16 v[50:65], v[130:133], v[210:213], v[50:65]
	ds_read_b64_tr_b16 v[210:211], v171 offset:0x600
	ds_read_b64_tr_b16 v[212:213], v171 offset:0xe00
	v_mfma_f32_32x32x16_bf16 v[50:65], v[134:137], v[214:217], v[50:65]
	ds_read_b64_tr_b16 v[214:215], v171 offset:0x1600
	ds_read_b64_tr_b16 v[216:217], v171 offset:0x1e00
	v_mfma_f32_32x32x16_bf16 v[50:65], v[138:141], v[218:221], v[50:65]
	ds_read_b64_tr_b16 v[218:219], v171 offset:0x2600
	ds_read_b64_tr_b16 v[220:221], v171 offset:0x2e00
	v_mfma_f32_32x32x16_bf16 v[50:65], v[142:145], v[222:225], v[50:65]
	ds_read_b64_tr_b16 v[222:223], v171 offset:0x3600
	ds_read_b64_tr_b16 v[224:225], v171 offset:0x3e00
	s_waitcnt lgkmcnt(8)
	s_nop 0
	s_waitcnt lgkmcnt(0)
	v_mfma_f32_32x32x16_bf16 v[34:49], v[130:133], v[176:179], v[34:49]
	v_mfma_f32_32x32x16_bf16 v[18:33], v[130:133], v[210:213], v[18:33]
	v_exp_f32_e32 v210, v105
	v_exp_f32_e32 v211, v111
	v_exp_f32_e32 v212, v113
	v_mfma_f32_32x32x16_bf16 v[34:49], v[134:137], v[198:201], v[34:49]
	v_exp_f32_e32 v200, v99
	v_exp_f32_e32 v198, v100
	v_exp_f32_e32 v199, v106
	v_exp_f32_e32 v201, v108
	v_mfma_f32_32x32x16_bf16 v[18:33], v[134:137], v[214:217], v[18:33]
	v_mfma_f32_32x32x16_bf16 v[34:49], v[138:141], v[202:205], v[34:49]
	v_exp_f32_e32 v202, v101
	v_exp_f32_e32 v204, v102
	v_exp_f32_e32 v205, v104
	v_exp_f32_e32 v203, v107
	v_mfma_f32_32x32x16_bf16 v[18:33], v[138:141], v[218:221], v[18:33]
	v_mfma_f32_32x32x16_bf16 v[34:49], v[142:145], v[206:209], v[34:49]
	v_exp_f32_e32 v207, v103
	v_exp_f32_e32 v209, v109
	v_exp_f32_e32 v206, v110
	v_exp_f32_e32 v208, v112
	v_mfma_f32_32x32x16_bf16 v[18:33], v[142:145], v[222:225], v[18:33]
	s_cmp_ge_u32 s57, s97
	s_cbranch_scc1 .LBB0_880

; __device__ __forceinline__ void finishSM(f32x16& p0, f32x16& p1, float& l_reg, bf16x8& pa0, bf16x8& pa1, bf16x8& pa2, bf16x8& pa3) {
; #pragma unroll
;   for (int r = 0; r < 16; ++r) p1[r] = __builtin_amdgcn_exp2f(p1[r]);
;   float ps = 0;
; #pragma unroll
;   for (int r = 0; r < 16; ++r) ps += p0[r];
; #pragma unroll
;   for (int r = 0; r < 16; ++r) ps += p1[r];
;   l_reg += ps;
;     ...
;   ATT_PK4(p0, 0, pa0); ATT_PK4(p0, 8, pa1); ATT_PK4(p1, 0, pa2); ATT_PK4(p1, 8, pa3);
;     ...
; }
; template <int DK>
; __device__ __forceinline__ void qkt(f32x16& p0, f32x16& p1, const char* Ks, const bf16x8* qr, int r32, int hi) {
;   p0 = f32x16{}; p1 = f32x16{};
; #pragma unroll
;   for (int d0 = 0; d0 < DK / 16; ++d0) { const int cb = (d0 * 16 + hi * 8) * 2;
;     const bf16x8 b0 = *reinterpret_cast<const bf16x8*>(Ks + ATT_KSWZ(r32, cb));
;     const bf16x8 b1 = *reinterpret_cast<const bf16x8*>(Ks + ATT_KSWZ(32 + r32, cb));
;     p0 = __builtin_amdgcn_mfma_f32_32x32x16_bf16(b0, qr[d0], p0, 0, 0, 0);
;     p1 = __builtin_amdgcn_mfma_f32_32x32x16_bf16(b1, qr[d0], p1, 0, 0, 0);
;   }
; }
; template <int DV, int GRP> __device__ __forceinline__ void v_group_read(s16x4* vf, int vb) {
;   sfor<0, 8>([&](auto ic) { constexpr int j = decltype(ic)::value; vf[j] = tr_read<v_rd_off<DV>(GRP, j / 2, j % 2)>(vb); });
; }
; __device__ __forceinline__ void pv_group(f32x16& od, const s16x4* vf, bf16x8 pa0, bf16x8 pa1, bf16x8 pa2, bf16x8 pa3) {
;     ...
;   od = __builtin_amdgcn_mfma_f32_32x32x16_bf16(pa0, ATT_PK(vf[0], vf[1]), od, 0, 0, 0);
;   od = __builtin_amdgcn_mfma_f32_32x32x16_bf16(pa1, ATT_PK(vf[2], vf[3]), od, 0, 0, 0);
;   od = __builtin_amdgcn_mfma_f32_32x32x16_bf16(pa2, ATT_PK(vf[4], vf[5]), od, 0, 0, 0);
;   od = __builtin_amdgcn_mfma_f32_32x32x16_bf16(pa3, ATT_PK(vf[6], vf[7]), od, 0, 0, 0);
;     ...
; }
; template <int DV> __device__ __forceinline__ void pv_all_pipe(f32x16* o, int vb, bf16x8 pa0, bf16x8 pa1, bf16x8 pa2, bf16x8 pa3) {
;   s16x4 va[8], vc[8];
;   v_group_read<DV, 0>(va, vb); v_group_read<DV, 1>(vc, vb);
;   lgkm_wait8<8>(va); pv_group(o[0], va, pa0, pa1, pa2, pa3);
;   if constexpr (DV == 128) {
;     s16x4 vd[8], ve[8];
;     v_group_read<DV, 2>(vd, vb);
;     lgkm_wait8<8>(vc); pv_group(o[1], vc, pa0, pa1, pa2, pa3);
;     v_group_read<DV, 3>(ve, vb);
;     lgkm_wait8<8>(vd); pv_group(o[2], vd, pa0, pa1, pa2, pa3);
;     lgkm_wait8<0>(ve); pv_group(o[3], ve, pa0, pa1, pa2, pa3);
.LBB0_879:
	ds_read_b128 v[66:69], v162
	ds_read_b128 v[70:73], v162 offset:4096
	ds_read_b128 v[130:133], v164
	ds_read_b128 v[134:137], v164 offset:4096
	v_exp_f32_e32 v82, v82
	v_exp_f32_e32 v83, v83
	v_add_f32_e32 v180, 0, v197
	v_add_f32_e32 v180, v200, v180
	v_add_f32_e32 v180, v198, v180
	v_add_f32_e32 v180, v202, v180
	v_add_f32_e32 v180, v204, v180
	v_add_f32_e32 v180, v207, v180
	v_add_f32_e32 v180, v205, v180
	v_add_f32_e32 v180, v210, v180
	v_add_f32_e32 v180, v199, v180
	v_add_f32_e32 v180, v203, v180
	v_add_f32_e32 v180, v201, v180
	v_add_f32_e32 v180, v209, v180
	v_add_f32_e32 v180, v206, v180
	v_add_f32_e32 v180, v211, v180
	v_add_f32_e32 v180, v208, v180
	v_add_f32_e32 v180, v212, v180
	s_waitcnt lgkmcnt(0)
	v_mfma_f32_32x32x16_bf16 v[98:113], v[66:69], v[114:117], 0
	v_exp_f32_e32 v84, v84
	v_exp_f32_e32 v85, v85
	v_exp_f32_e32 v86, v86
	v_exp_f32_e32 v87, v87
	v_exp_f32_e32 v88, v88
	v_exp_f32_e32 v89, v89
	v_exp_f32_e32 v90, v90
	v_mfma_f32_32x32x16_bf16 v[66:81], v[70:73], v[114:117], 0
	s_cmp_eq_u32 s80, 0
	s_cbranch_scc1 .Lstg_l4
	s_cmp_ge_u32 s55, s95
	s_cbranch_scc1 .Lstg_l4
	s_add_u32 s98, s76, 0x1ec0c000
	s_addc_u32 s99, s77, 0
	s_mov_b32 m0, s89
	s_nop 0
	global_load_lds_dwordx4 v0, s[98:99]
	s_add_u32 s98, s78, 0xdcc1000
	s_addc_u32 s99, s79, 0
	s_mov_b32 m0, s91
	s_nop 0
	global_load_lds_dwordx4 v232, s[98:99]
	s_add_u32 s98, s98, 0x80
	s_addc_u32 s99, s99, 0
	s_mov_b32 m0, s92
	s_nop 0
	global_load_lds_dwordx4 v232, s[98:99]
.Lstg_l4:
	v_exp_f32_e32 v91, v91
	v_exp_f32_e32 v92, v92
	v_exp_f32_e32 v93, v93
	v_exp_f32_e32 v94, v94
	v_exp_f32_e32 v95, v95
	v_exp_f32_e32 v96, v96
	v_exp_f32_e32 v97, v97
	v_mfma_f32_32x32x16_bf16 v[98:113], v[130:133], v[118:121], v[98:113]
	v_mfma_f32_32x32x16_bf16 v[66:81], v[134:137], v[118:121], v[66:81]
	ds_read_b128 v[130:133], v166
	ds_read_b128 v[134:137], v166 offset:4096
	v_add_f32_e32 v180, v82, v180
	v_add_f32_e32 v180, v83, v180
	v_add_f32_e32 v180, v84, v180
	v_add_f32_e32 v180, v85, v180
	v_add_f32_e32 v180, v86, v180
	v_add_f32_e32 v180, v87, v180
	v_add_f32_e32 v180, v88, v180
	v_add_f32_e32 v180, v89, v180
	s_waitcnt lgkmcnt(0)
	v_mfma_f32_32x32x16_bf16 v[98:113], v[130:133], v[122:125], v[98:113]
	v_mfma_f32_32x32x16_bf16 v[66:81], v[134:137], v[122:125], v[66:81]
	ds_read_b128 v[130:133], v168
	ds_read_b128 v[134:137], v168 offset:4096
	v_add_f32_e32 v180, v90, v180
	v_add_f32_e32 v180, v91, v180
	v_add_f32_e32 v180, v92, v180
	v_add_f32_e32 v180, v93, v180
	v_add_f32_e32 v180, v94, v180
	v_add_f32_e32 v180, v95, v180
	v_add_f32_e32 v180, v96, v180
	v_add_f32_e32 v180, v97, v180
	s_waitcnt lgkmcnt(0)
	v_mfma_f32_32x32x16_bf16 v[98:113], v[130:133], v[126:129], v[98:113]
	v_mfma_f32_32x32x16_bf16 v[66:81], v[134:137], v[126:129], v[66:81]
	v_add_f32_e32 v172, v172, v180
	v_cvt_pk_bf16_f32 v130, v197, v200
	v_cvt_pk_bf16_f32 v131, v198, v202
	v_cvt_pk_bf16_f32 v132, v204, v207
	v_cvt_pk_bf16_f32 v133, v205, v210
	v_cvt_pk_bf16_f32 v134, v199, v203
	v_cvt_pk_bf16_f32 v135, v201, v209
	v_cvt_pk_bf16_f32 v136, v206, v211
	v_cvt_pk_bf16_f32 v137, v208, v212
	v_cvt_pk_bf16_f32 v138, v82, v83
	v_cvt_pk_bf16_f32 v139, v84, v85
	v_cvt_pk_bf16_f32 v140, v86, v87
	v_cvt_pk_bf16_f32 v141, v88, v89
	v_cvt_pk_bf16_f32 v142, v90, v91
	v_cvt_pk_bf16_f32 v143, v92, v93
	v_cvt_pk_bf16_f32 v144, v94, v95
	v_cvt_pk_bf16_f32 v145, v96, v97
	ds_read_b64_tr_b16 v[174:175], v160 offset:0
	ds_read_b64_tr_b16 v[176:177], v160 offset:0x800
	ds_read_b64_tr_b16 v[184:185], v160 offset:0x1000
	ds_read_b64_tr_b16 v[186:187], v160 offset:0x1800
	ds_read_b64_tr_b16 v[188:189], v160 offset:0x2000
	ds_read_b64_tr_b16 v[190:191], v160 offset:0x2800
	ds_read_b64_tr_b16 v[192:193], v160 offset:0x3000
	ds_read_b64_tr_b16 v[194:195], v160 offset:0x3800
	ds_read_b64_tr_b16 v[214:215], v160 offset:0x200
	ds_read_b64_tr_b16 v[216:217], v160 offset:0xa00
	ds_read_b64_tr_b16 v[218:219], v160 offset:0x1200
	s_nop 0
	v_permlane32_swap_b32_e32 v130, v132
	v_permlane32_swap_b32_e32 v131, v133
	ds_read_b64_tr_b16 v[220:221], v160 offset:0x1a00
	ds_read_b64_tr_b16 v[222:223], v160 offset:0x2200
	ds_read_b64_tr_b16 v[224:225], v160 offset:0x2a00
	ds_read_b64_tr_b16 v[226:227], v160 offset:0x3200
	ds_read_b64_tr_b16 v[228:229], v160 offset:0x3a00
	s_waitcnt lgkmcnt(8)
	v_permlane32_swap_b32_e32 v134, v136
	s_nop 0
	v_mfma_f32_32x32x16_bf16 v[2:17], v[130:133], v[174:177], v[2:17]
	v_permlane32_swap_b32_e32 v135, v137
	v_permlane32_swap_b32_e32 v138, v140
	v_permlane32_swap_b32_e32 v139, v141
	ds_read_b64_tr_b16 v[174:175], v160 offset:0x400
	v_mfma_f32_32x32x16_bf16 v[2:17], v[134:137], v[184:187], v[2:17]
	v_permlane32_swap_b32_e32 v142, v144
	v_permlane32_swap_b32_e32 v143, v145
	ds_read_b64_tr_b16 v[176:177], v160 offset:0xc00
	ds_read_b64_tr_b16 v[184:185], v160 offset:0x1400
	ds_read_b64_tr_b16 v[186:187], v160 offset:0x1c00
	v_mfma_f32_32x32x16_bf16 v[2:17], v[138:141], v[188:191], v[2:17]
	ds_read_b64_tr_b16 v[188:189], v160 offset:0x2400
	ds_read_b64_tr_b16 v[190:191], v160 offset:0x2c00
	v_exp_f32_e32 v173, v98
	v_exp_f32_e32 v196, v113
	v_mfma_f32_32x32x16_bf16 v[2:17], v[142:145], v[192:195], v[2:17]
	ds_read_b64_tr_b16 v[192:193], v160 offset:0x3400
	ds_read_b64_tr_b16 v[194:195], v160 offset:0x3c00
	s_waitcnt lgkmcnt(8)
	s_nop 0
	v_mfma_f32_32x32x16_bf16 v[50:65], v[130:133], v[214:217], v[50:65]
	ds_read_b64_tr_b16 v[214:215], v160 offset:0x600
	ds_read_b64_tr_b16 v[216:217], v160 offset:0xe00
	v_mfma_f32_32x32x16_bf16 v[50:65], v[134:137], v[218:221], v[50:65]
	ds_read_b64_tr_b16 v[218:219], v160 offset:0x1600
	ds_read_b64_tr_b16 v[220:221], v160 offset:0x1e00
	v_mfma_f32_32x32x16_bf16 v[50:65], v[138:141], v[222:225], v[50:65]
	ds_read_b64_tr_b16 v[222:223], v160 offset:0x2600
	ds_read_b64_tr_b16 v[224:225], v160 offset:0x2e00
	v_mfma_f32_32x32x16_bf16 v[50:65], v[142:145], v[226:229], v[50:65]
	ds_read_b64_tr_b16 v[226:227], v160 offset:0x3600
	ds_read_b64_tr_b16 v[228:229], v160 offset:0x3e00
	s_waitcnt lgkmcnt(8)
	s_nop 0
	s_waitcnt lgkmcnt(0)
	v_mfma_f32_32x32x16_bf16 v[34:49], v[130:133], v[174:177], v[34:49]
	v_exp_f32_e32 v174, v99
	v_exp_f32_e32 v175, v100
	v_mfma_f32_32x32x16_bf16 v[18:33], v[130:133], v[214:217], v[18:33]
	v_mfma_f32_32x32x16_bf16 v[34:49], v[134:137], v[184:187], v[34:49]
	v_exp_f32_e32 v184, v101
	v_exp_f32_e32 v185, v102
	v_exp_f32_e32 v186, v103
	v_exp_f32_e32 v187, v104
	v_mfma_f32_32x32x16_bf16 v[18:33], v[134:137], v[218:221], v[18:33]
	v_mfma_f32_32x32x16_bf16 v[34:49], v[138:141], v[188:191], v[34:49]
	v_exp_f32_e32 v188, v105
	v_exp_f32_e32 v189, v106
	v_exp_f32_e32 v190, v107
	v_exp_f32_e32 v191, v108
	v_mfma_f32_32x32x16_bf16 v[18:33], v[138:141], v[222:225], v[18:33]
	v_mfma_f32_32x32x16_bf16 v[34:49], v[142:145], v[192:195], v[34:49]
	v_exp_f32_e32 v192, v109
	v_exp_f32_e32 v193, v110
	v_exp_f32_e32 v194, v111
	v_exp_f32_e32 v195, v112
	v_mfma_f32_32x32x16_bf16 v[18:33], v[142:145], v[226:229], v[18:33]
